# dense GEMM unit heads (in-proj/out-proj/moe_dn): deleted the per-unit recomputation of the unit-independent A staging offsets (52 VALU each; the 4 v_mov copies already carry them) on top of v59
# speedup vs baseline: 1.0082x; 1.0009x over previous
.LBB0_535:
	s_or_b64 exec, exec, s[2:3]
	s_andn2_b64 vcc, exec, s[20:21]
	v_mov_b32_e32 v217, v174
	v_mov_b32_e32 v215, v168
	v_mov_b32_e32 v216, v176
	v_mov_b32_e32 v214, v170
	s_mov_b64 s[16:17], s[26:27]
	s_mov_b64 s[18:19], s[24:25]
	s_cbranch_vccnz .LBB0_537
	s_mov_b64 s[16:17], s[10:11]
	s_mov_b64 s[18:19], s[8:9]

.LBB0_1316:
	s_mov_b32 s97, s95
	s_mov_b32 s84, s94
	s_or_b64 exec, exec, s[16:17]
	s_andn2_b64 vcc, exec, s[20:21]
	v_mov_b32_e32 v195, v132
	v_mov_b32_e32 v193, v128
	v_mov_b32_e32 v194, v134
	v_mov_b32_e32 v192, v130
	s_mov_b64 s[16:17], s[28:29]
	s_mov_b64 s[18:19], s[26:27]
	s_cbranch_vccnz .LBB0_1318
	s_mov_b64 s[16:17], s[12:13]
	s_mov_b64 s[18:19], s[10:11]

.LBB0_1663:
	s_or_b64 exec, exec, s[16:17]
	s_andn2_b64 vcc, exec, s[20:21]
	v_mov_b32_e32 v214, v170
	v_mov_b32_e32 v196, v166
	v_mov_b32_e32 v197, v174
	v_mov_b32_e32 v195, v168
	s_mov_b64 s[16:17], s[24:25]
	s_mov_b64 s[18:19], s[22:23]
	s_cbranch_vccnz .LBB0_1665
	s_mov_b64 s[16:17], s[8:9]
	s_mov_b64 s[18:19], s[10:11]
